# k_gcn prologue latency chain: rows_0 issued before the max-degree reduction, second-phase kernarg s_loads hoisted to the top
# baseline (speedup 1.0000x reference)
_Z5k_gcnILi128ELb1ELi16EEvPKDv8_DF16_PKiS4_PKfS2_S6_PDF16_S6_S6_S2_S6_S2_S6_S6_S6_PfS4_:
	s_load_dwordx4 s[20:23], s[0:1], 0x8
	s_load_dwordx2 s[4:5], s[0:1], 0x20
	s_lshl_b32 s29, s2, 4
	s_load_dwordx2 s[24:25], s[0:1], 0x0
	s_load_dwordx2 s[2:3], s[0:1], 0x18
	v_readfirstlane_b32 s30, v0
	v_and_b32_e32 v1, 63, v0
	s_lshr_b32 s28, s30, 6
	v_lshl_or_b32 v2, s28, 9, v1
	v_mov_b32_e32 v3, 0
	v_bfe_u32 v83, v0, 4, 2
	s_waitcnt lgkmcnt(0)
	v_lshl_add_u64 v[14:15], v[2:3], 4, s[4:5]
	v_ashrrev_i32_e32 v3, 31, v2
	s_lshl_b32 s6, s28, 2
	v_or_b32_e32 v38, s29, v83
	v_add_lshl_u32 v38, v38, s6, 2
	global_load_dwordx2 v[50:51], v38, s[20:21]
	v_lshl_add_u64 v[16:17], v[2:3], 4, s[4:5]
	global_load_dwordx4 v[26:29], v[14:15], off
	global_load_dwordx4 v[10:13], v[16:17], off offset:1024
	global_load_dwordx4 v[6:9], v[16:17], off offset:2048
	global_load_dwordx4 v[2:5], v[16:17], off offset:3072
	v_or_b32_e32 v14, s29, v83
	s_lshl_b32 s6, s28, 2
	v_add_u32_e32 v14, s6, v14
	s_movk_i32 s31, 0x1000
	v_ashrrev_i32_e32 v15, 31, v14
	v_add_co_u32_e32 v34, vcc, s31, v16
	v_lshl_add_u64 v[36:37], v[14:15], 2, s[20:21]
	s_nop 0
	v_addc_co_u32_e32 v35, vcc, 0, v17, vcc
	global_load_dwordx4 v[30:33], v[34:35], off
	global_load_dwordx4 v[22:25], v[34:35], off offset:1024
	global_load_dwordx4 v[18:21], v[34:35], off offset:2048
	global_load_dwordx4 v[14:17], v[34:35], off offset:3072
	s_waitcnt vmcnt(8)
	v_sub_u32_e32 v53, v51, v50
	v_lshlrev_b32_e32 v34, 2, v50
	global_load_dword v36, v34, s[22:23]
	global_load_dword v38, v34, s[22:23] offset:4
	global_load_dword v42, v34, s[22:23] offset:8
	global_load_dword v46, v34, s[22:23] offset:12
	v_and_b32_e32 v82, 15, v0
	v_or_b32_e32 v51, s6, v83
	v_add_u32_e32 v34, s29, v51
	v_lshlrev_b32_e32 v54, 4, v82
	s_mov_b32 s27, 0x20000
	s_mov_b32 s26, 0x4e2100
	s_waitcnt lgkmcnt(0)
	s_and_b32 s25, s25, 0xffff
	v_lshl_or_b32 v35, v34, 8, v54
	buffer_load_dwordx4 v[64:67], v35, s[24:27], 0 offen
	v_ashrrev_i32_e32 v35, 31, v34
	v_lshl_add_u64 v[34:35], v[34:35], 2, s[2:3]
	global_load_dword v52, v[34:35], off
	v_mbcnt_lo_u32_b32 v34, -1, 0
	v_mbcnt_hi_u32_b32 v34, -1, v34
	v_and_b32_e32 v37, 64, v34
	v_xor_b32_e32 v35, 32, v34
	v_add_u32_e32 v37, 64, v37
	v_cmp_lt_i32_e32 vcc, v35, v37
	v_xor_b32_e32 v39, 16, v34
	s_load_dwordx2 s[2:3], s[0:1], 0x78
	s_load_dwordx8 s[4:11], s[0:1], 0x58
	s_load_dwordx8 s[12:19], s[0:1], 0x38
	v_cndmask_b32_e32 v35, v34, v35, vcc
	v_lshlrev_b32_e32 v84, 2, v35
	ds_bpermute_b32 v73, v84, v53
	v_cmp_lt_i32_e32 vcc, v39, v37
	s_mov_b32 s33, 4
	s_waitcnt vmcnt(1)
	v_mov_b32_e32 v70, 0x4e20
	v_cmp_lt_i32_e64 s[34:35], 0, v53
	v_cmp_lt_i32_e64 s[36:37], 1, v53
	v_cmp_lt_i32_e64 s[38:39], 2, v53
	v_cmp_lt_i32_e64 s[40:41], 3, v53
	v_cndmask_b32_e64 v36, v70, v36, s[34:35]
	v_cndmask_b32_e64 v38, v70, v38, s[36:37]
	v_cndmask_b32_e64 v42, v70, v42, s[38:39]
	v_cndmask_b32_e64 v46, v70, v46, s[40:41]
	v_cvt_f32_f16_e32 v62, v64
	v_cndmask_b32_e32 v34, v34, v39, vcc
	v_lshlrev_b32_e32 v85, 2, v34
	v_lshl_or_b32 v34, v36, 8, v54
	buffer_load_dwordx4 v[34:37], v34, s[24:27], 0 offen
	v_lshl_or_b32 v38, v38, 8, v54
	buffer_load_dwordx4 v[38:41], v38, s[24:27], 0 offen
	v_lshl_or_b32 v42, v42, 8, v54
	buffer_load_dwordx4 v[42:45], v42, s[24:27], 0 offen
	v_lshl_or_b32 v46, v46, 8, v54
	buffer_load_dwordx4 v[46:49], v46, s[24:27], 0 offen
	s_waitcnt lgkmcnt(0)
	v_cmp_gt_u32_e64 s[36:37], 16, v0
	s_and_saveexec_b64 s[38:39], s[36:37]
	s_cbranch_execz .Lkg_tail_skip
	v_or_b32_e32 v80, s29, v0
	v_mul_u32_u24_e32 v81, 0x108, v80
	v_lshlrev_b32_e32 v94, 2, v80
	global_load_dwordx2 v[80:81], v81, s[12:13]
	global_load_dword v94, v94, s[14:15]
.Lkg_tail_skip:
	s_mov_b64 exec, s[38:39]
	v_max_i32_e32 v72, v53, v73
	ds_bpermute_b32 v73, v85, v72
	v_cvt_f32_f16_sdwa v63, v64 dst_sel:DWORD dst_unused:UNUSED_PAD src0_sel:WORD_1
	v_cvt_f32_f16_e32 v60, v65
	v_cvt_f32_f16_sdwa v61, v65 dst_sel:DWORD dst_unused:UNUSED_PAD src0_sel:WORD_1
	v_cvt_f32_f16_e32 v58, v66
	v_cvt_f32_f16_sdwa v59, v66 dst_sel:DWORD dst_unused:UNUSED_PAD src0_sel:WORD_1
	v_cvt_f32_f16_e32 v56, v67
	v_cvt_f32_f16_sdwa v57, v67 dst_sel:DWORD dst_unused:UNUSED_PAD src0_sel:WORD_1
	s_waitcnt lgkmcnt(0)
	v_max_i32_e32 v72, v72, v73
	s_nop 0
	v_readfirstlane_b32 s31, v72
	s_cmp_lt_i32 s31, 1
	s_cbranch_scc1 .Lkg_skip0
.LBB2_9:
	v_add_lshl_u32 v68, v50, s33, 2
	v_subrev_u32_e32 v69, s33, v53
	global_load_dword v64, v68, s[22:23]
	global_load_dword v55, v68, s[22:23] offset:4
	global_load_dword v66, v68, s[22:23] offset:8
	global_load_dword v65, v68, s[22:23] offset:12

.Lkg_skip0:
	s_waitcnt vmcnt(0)
	s_branch .LBB2_19
